# bias wait of the first in-projection GEMM epilogue counted (vmcnt(8)) like the other GEMMs; on top of thin w2 conversion slots in expert GEMM 1
# baseline (speedup 1.0000x reference)
.LBB0_239:
	v_mov_b32_e32 v150, v182
	s_lshl_b32 s21, s76, 8
	v_readfirstlane_b32 s19, v150
	s_ashr_i32 s76, s19, 2
	s_andn2_b32 s76, s76, 63
	s_lshr_b32 s19, s19, 1
	s_add_i32 s76, s76, s21
	s_lshl_b32 s21, s26, 8
	s_and_b32 s19, s19, 0x60
	v_and_or_b32 v172, v150, 15, s76
	s_or_b32 s19, s19, s21
	v_lshrrev_b32_e32 v150, 1, v150
	v_and_or_b32 v152, v150, 24, s19
	v_ashrrev_i32_e32 v153, 31, v152
	v_mov_b64_e32 v[150:151], s[8:9]
	v_mad_i64_i32 v[168:169], s[78:79], v172, s67, v[150:151]
	v_lshlrev_b64 v[152:153], 1, v[152:153]
	s_waitcnt vmcnt(8)
	v_pk_add_f32 v[148:149], v[16:17], v[148:149]
	v_pk_add_f32 v[146:147], v[14:15], v[146:147]
	v_pk_add_f32 v[170:171], v[12:13], v[144:145]
	v_pk_add_f32 v[144:145], v[10:11], v[142:143]
	v_lshl_add_u64 v[168:169], v[168:169], 0, v[152:153]
	v_cvt_pk_bf16_f32 v142, v146, v147
	v_cvt_pk_bf16_f32 v143, v148, v149
	v_cvt_pk_bf16_f32 v144, v144, v145
	v_cvt_pk_bf16_f32 v145, v170, v171
	global_store_dwordx4 v[168:169], v[142:145], off
	v_pk_add_f32 v[136:137], v[8:9], v[136:137]
	v_pk_add_f32 v[134:135], v[6:7], v[134:135]
	v_pk_add_f32 v[142:143], v[4:5], v[128:129]
	v_pk_add_f32 v[128:129], v[2:3], v[126:127]
	v_cvt_pk_bf16_f32 v126, v134, v135
	v_cvt_pk_bf16_f32 v127, v136, v137
	v_cvt_pk_bf16_f32 v128, v128, v129
	v_cvt_pk_bf16_f32 v129, v142, v143
	global_store_dwordx4 v[168:169], v[126:129], off offset:256
	v_pk_add_f32 v[132:133], v[12:13], v[132:133]
	v_pk_add_f32 v[130:131], v[10:11], v[130:131]
	v_or_b32_e32 v126, 16, v172
	v_mad_i64_i32 v[126:127], s[78:79], v126, s67, v[150:151]
	v_lshl_add_u64 v[134:135], v[126:127], 0, v[152:153]
	v_pk_add_f32 v[128:129], v[16:17], v[140:141]
	v_pk_add_f32 v[126:127], v[14:15], v[138:139]
	v_pk_add_f32 v[120:121], v[8:9], v[120:121]
	v_cvt_pk_bf16_f32 v126, v126, v127
	v_cvt_pk_bf16_f32 v127, v128, v129
	v_cvt_pk_bf16_f32 v128, v130, v131
	v_cvt_pk_bf16_f32 v129, v132, v133
	global_store_dwordx4 v[134:135], v[126:129], off
	v_pk_add_f32 v[118:119], v[6:7], v[118:119]
	v_pk_add_f32 v[116:117], v[12:13], v[116:117]
	v_pk_add_f32 v[126:127], v[4:5], v[112:113]
	v_pk_add_f32 v[112:113], v[2:3], v[110:111]
	v_cvt_pk_bf16_f32 v110, v118, v119
	v_cvt_pk_bf16_f32 v111, v120, v121
	v_cvt_pk_bf16_f32 v112, v112, v113
	v_cvt_pk_bf16_f32 v113, v126, v127
	global_store_dwordx4 v[134:135], v[110:113], off offset:256
	v_pk_add_f32 v[114:115], v[10:11], v[114:115]
	v_pk_add_f32 v[104:105], v[8:9], v[104:105]
	v_or_b32_e32 v110, 32, v172
	v_mad_i64_i32 v[110:111], s[78:79], v110, s67, v[150:151]
	v_lshl_add_u64 v[118:119], v[110:111], 0, v[152:153]
	v_pk_add_f32 v[112:113], v[16:17], v[124:125]
	v_pk_add_f32 v[110:111], v[14:15], v[122:123]
	v_pk_add_f32 v[102:103], v[6:7], v[102:103]
	v_cvt_pk_bf16_f32 v110, v110, v111
	v_cvt_pk_bf16_f32 v111, v112, v113
	v_cvt_pk_bf16_f32 v112, v114, v115
	v_cvt_pk_bf16_f32 v113, v116, v117
	global_store_dwordx4 v[118:119], v[110:113], off
	v_pk_add_f32 v[100:101], v[12:13], v[100:101]
	v_pk_add_f32 v[98:99], v[10:11], v[98:99]
	v_pk_add_f32 v[110:111], v[4:5], v[96:97]
	v_pk_add_f32 v[96:97], v[2:3], v[94:95]
	v_cvt_pk_bf16_f32 v94, v102, v103
	v_cvt_pk_bf16_f32 v95, v104, v105
	v_cvt_pk_bf16_f32 v96, v96, v97
	v_cvt_pk_bf16_f32 v97, v110, v111
	global_store_dwordx4 v[118:119], v[94:97], off offset:256
	v_pk_add_f32 v[92:93], v[8:9], v[92:93]
	v_pk_add_f32 v[90:91], v[6:7], v[90:91]
	v_or_b32_e32 v94, 48, v172
	v_mad_i64_i32 v[94:95], s[78:79], v94, s67, v[150:151]
	v_lshl_add_u64 v[102:103], v[94:95], 0, v[152:153]
	v_pk_add_f32 v[96:97], v[16:17], v[108:109]
	v_pk_add_f32 v[94:95], v[14:15], v[106:107]
	v_pk_add_f32 v[84:85], v[16:17], v[84:85]
	v_cvt_pk_bf16_f32 v94, v94, v95
	v_cvt_pk_bf16_f32 v95, v96, v97
	v_cvt_pk_bf16_f32 v96, v98, v99
	v_cvt_pk_bf16_f32 v97, v100, v101
	global_store_dwordx4 v[102:103], v[94:97], off
	v_pk_add_f32 v[82:83], v[14:15], v[82:83]
	v_pk_add_f32 v[72:73], v[8:9], v[72:73]
	v_pk_add_f32 v[94:95], v[4:5], v[88:89]
	v_pk_add_f32 v[88:89], v[2:3], v[86:87]
	v_cvt_pk_bf16_f32 v86, v90, v91
	v_cvt_pk_bf16_f32 v87, v92, v93
	v_cvt_pk_bf16_f32 v88, v88, v89
	v_cvt_pk_bf16_f32 v89, v94, v95
	global_store_dwordx4 v[102:103], v[86:89], off offset:256
	v_pk_add_f32 v[70:71], v[6:7], v[70:71]
	v_pk_add_f32 v[64:65], v[12:13], v[64:65]
	v_add_u32_e32 v86, 0x80, v172
	v_mad_i64_i32 v[86:87], s[78:79], v86, s67, v[150:151]
	v_pk_add_f32 v[88:89], v[12:13], v[80:81]
	v_pk_add_f32 v[80:81], v[10:11], v[78:79]
	v_lshl_add_u64 v[86:87], v[86:87], 0, v[152:153]
	v_cvt_pk_bf16_f32 v78, v82, v83
	v_cvt_pk_bf16_f32 v79, v84, v85
	v_cvt_pk_bf16_f32 v80, v80, v81
	v_cvt_pk_bf16_f32 v81, v88, v89
	global_store_dwordx4 v[86:87], v[78:81], off
	v_pk_add_f32 v[62:63], v[10:11], v[62:63]
	v_pk_add_f32 v[52:53], v[8:9], v[52:53]
	v_pk_add_f32 v[78:79], v[4:5], v[60:61]
	v_pk_add_f32 v[60:61], v[2:3], v[58:59]
	v_cvt_pk_bf16_f32 v58, v70, v71
	v_cvt_pk_bf16_f32 v59, v72, v73
	v_cvt_pk_bf16_f32 v60, v60, v61
	v_cvt_pk_bf16_f32 v61, v78, v79
	global_store_dwordx4 v[86:87], v[58:61], off offset:256
	v_pk_add_f32 v[50:51], v[6:7], v[50:51]
	v_pk_add_f32 v[48:49], v[12:13], v[48:49]
	v_add_u32_e32 v58, 0x90, v172
	v_mad_i64_i32 v[58:59], s[78:79], v58, s67, v[150:151]
	v_lshl_add_u64 v[70:71], v[58:59], 0, v[152:153]
	v_pk_add_f32 v[60:61], v[16:17], v[76:77]
	v_pk_add_f32 v[58:59], v[14:15], v[74:75]
	v_pk_add_f32 v[46:47], v[10:11], v[46:47]
	v_cvt_pk_bf16_f32 v58, v58, v59
	v_cvt_pk_bf16_f32 v59, v60, v61
	v_cvt_pk_bf16_f32 v60, v62, v63
	v_cvt_pk_bf16_f32 v61, v64, v65
	global_store_dwordx4 v[70:71], v[58:61], off
	v_pk_add_f32 v[36:37], v[8:9], v[36:37]
	v_pk_add_f32 v[34:35], v[6:7], v[34:35]
	v_pk_add_f32 v[58:59], v[4:5], v[44:45]
	v_pk_add_f32 v[44:45], v[2:3], v[42:43]
	v_cvt_pk_bf16_f32 v42, v50, v51
	v_cvt_pk_bf16_f32 v43, v52, v53
	v_cvt_pk_bf16_f32 v44, v44, v45
	v_cvt_pk_bf16_f32 v45, v58, v59
	global_store_dwordx4 v[70:71], v[42:45], off offset:256
	v_pk_add_f32 v[8:9], v[8:9], v[24:25]
	v_pk_add_f32 v[6:7], v[6:7], v[22:23]
	v_add_u32_e32 v42, 0xa0, v172
	v_mad_i64_i32 v[42:43], s[78:79], v42, s67, v[150:151]
	v_lshl_add_u64 v[50:51], v[42:43], 0, v[152:153]
	v_pk_add_f32 v[44:45], v[16:17], v[56:57]
	v_pk_add_f32 v[42:43], v[14:15], v[54:55]
	v_pk_add_f32 v[16:17], v[16:17], v[40:41]
	v_cvt_pk_bf16_f32 v42, v42, v43
	v_cvt_pk_bf16_f32 v43, v44, v45
	v_cvt_pk_bf16_f32 v44, v46, v47
	v_cvt_pk_bf16_f32 v45, v48, v49
	global_store_dwordx4 v[50:51], v[42:45], off
	v_pk_add_f32 v[14:15], v[14:15], v[38:39]
	s_andn2_b64 vcc, exec, s[4:5]
	v_pk_add_f32 v[42:43], v[4:5], v[28:29]
	v_pk_add_f32 v[28:29], v[2:3], v[26:27]
	v_cvt_pk_bf16_f32 v26, v34, v35
	v_cvt_pk_bf16_f32 v27, v36, v37
	v_cvt_pk_bf16_f32 v28, v28, v29
	v_cvt_pk_bf16_f32 v29, v42, v43
	global_store_dwordx4 v[50:51], v[26:29], off offset:256
	s_mov_b64 s[4:5], -1
	s_nop 0
	v_add_u32_e32 v26, 0xb0, v172
	v_mad_i64_i32 v[26:27], s[78:79], v26, s67, v[150:151]
	v_pk_add_f32 v[28:29], v[12:13], v[32:33]
	v_pk_add_f32 v[12:13], v[10:11], v[30:31]
	v_lshl_add_u64 v[26:27], v[26:27], 0, v[152:153]
	v_cvt_pk_bf16_f32 v10, v14, v15
	v_cvt_pk_bf16_f32 v11, v16, v17
	v_cvt_pk_bf16_f32 v12, v12, v13
	v_cvt_pk_bf16_f32 v13, v28, v29
	global_store_dwordx4 v[26:27], v[10:13], off
	s_nop 1
	v_pk_add_f32 v[10:11], v[4:5], v[20:21]
	v_pk_add_f32 v[4:5], v[2:3], v[18:19]
	v_cvt_pk_bf16_f32 v2, v6, v7
	v_cvt_pk_bf16_f32 v3, v8, v9
	v_cvt_pk_bf16_f32 v4, v4, v5
	v_cvt_pk_bf16_f32 v5, v10, v11
	global_store_dwordx4 v[26:27], v[2:5], off offset:256
	s_cbranch_vccnz .LBB0_228
	s_nop 0
	v_lshl_or_b32 v2, s20, 8, v166
	v_ashrrev_i32_e32 v3, 31, v2
	v_lshl_add_u64 v[6:7], v[2:3], 2, s[10:11]
	global_load_dwordx4 v[10:13], v[6:7], off offset:16
	global_load_dwordx4 v[14:17], v[6:7], off
	global_load_dwordx4 v[2:5], v[6:7], off offset:528
	s_nop 0
	global_load_dwordx4 v[6:9], v[6:7], off offset:512
	s_andn2_b64 vcc, exec, s[14:15]
	s_cbranch_vccnz .LBB0_227
	s_barrier
	s_branch .LBB0_227
